# attention-A side-work DMA: row step folded into the lane offset register (no 64-bit scalar pointer add per tile)
# speedup vs baseline: 1.0105x; 1.0000x over previous
.LBB0_417:
	s_add_i32 m0, s89, 0x2000
	s_barrier
	global_load_lds_dwordx4 v164, s[10:11]
	v_add_u32_e32 v164, 0x2000, v164
	s_add_i32 m0, s89, 0x8000
	s_add_i32 s100, s100, 0x400
	global_load_lds_dwordx4 v174, s[16:17]
	v_add_u32_e32 v174, 0x2000, v174
	s_mov_b32 m0, s100
	v_add_u32_e32 v96, -16, v215
	v_bfi_b32 v96, s15, v96, v215
	v_add_u32_e32 v215, s101, v96
	global_load_lds_dwordx4 v215, s[98:99] nt

.LBB0_428:
	s_mov_b32 m0, s89
	s_barrier
	global_load_lds_dwordx4 v164, s[10:11]
	v_add_u32_e32 v164, 0x2000, v164
	s_add_i32 m0, s89, 0x6000
	s_bfe_u32 s4, s1, 0x30000
	global_load_lds_dwordx4 v174, s[16:17]
	v_add_u32_e32 v174, 0x2000, v174
	s_cbranch_scc0 .LBB0_432
	s_add_i32 s100, s100, 0x400
	s_mov_b32 m0, s100
	v_add_u32_e32 v128, -16, v215
	v_bfi_b32 v128, s15, v128, v215
	v_add_u32_e32 v215, s101, v128
	global_load_lds_dwordx4 v215, s[98:99] nt
